# baseline (speedup 1.0000x reference)
.LBB0_22:
	s_andn2_b64 vcc, exec, s[4:5]
	s_cbranch_vccnz .LBB0_83
	s_movk_i32 s3, 0x200
	v_cmp_gt_u32_e32 vcc, s3, v0
	s_and_saveexec_b64 s[4:5], vcc
	v_mov_b32_e32 v1, 0x10200
	v_lshl_add_u32 v1, v0, 2, v1
	v_mov_b32_e32 v2, 0
	ds_write_b32 v1, v2
	s_or_b64 exec, exec, s[4:5]
	s_load_dwordx4 s[4:7], s[0:1], 0x40
	s_mul_i32 s20, s2, 0x1e85
	s_min_i32 s3, s20, 0xf23bb
	s_add_i32 s21, s3, 0x1e85
	v_add_u32_e32 v26, s20, v0
	v_mov_b32_e32 v2, 0
	v_cmp_gt_i32_e32 vcc, s21, v26
	v_mov_b32_e32 v3, v2
	v_mov_b32_e32 v4, v2
	v_mov_b32_e32 v5, v2
	v_mov_b32_e32 v6, v2
	v_mov_b32_e32 v7, v2
	v_mov_b32_e32 v8, v2
	v_mov_b32_e32 v9, v2
	v_mov_b32_e32 v1, -1
	v_mov_b32_e32 v30, -1
	s_waitcnt lgkmcnt(0)
	s_barrier
	s_and_saveexec_b64 s[8:9], vcc
	s_cbranch_execz .LBB0_27
	v_ashrrev_i32_e32 v27, 31, v26
	v_lshlrev_b64 v[10:11], 2, v[26:27]
	v_lshl_add_u64 v[12:13], s[4:5], 0, v[10:11]
	v_lshl_add_u64 v[10:11], s[6:7], 0, v[10:11]
	global_load_dword v2, v[12:13], off
	global_load_dword v30, v[10:11], off

.LBB0_41:
	s_or_b64 exec, exec, s[8:9]
	v_mov_b32_e32 v10, 0
	v_mov_b32_e32 v16, v10
	v_mov_b32_e32 v17, v10
	v_mov_b32_e32 v11, v10
	v_mov_b32_e32 v12, v10
	v_mov_b32_e32 v13, v10
	v_mov_b32_e32 v14, v10
	v_mov_b32_e32 v15, v10
	v_mov_b64_e32 v[24:25], v[16:17]
	s_waitcnt vmcnt(0)
	v_cmp_lt_i32_e32 vcc, -1, v30
	v_ashrrev_i32_e32 v34, 9, v2
	v_lshrrev_b32_e32 v35, 7, v30
	v_mov_b64_e32 v[22:23], v[14:15]
	v_mov_b64_e32 v[20:21], v[12:13]
	v_mov_b64_e32 v[18:19], v[10:11]
	s_and_saveexec_b64 s[4:5], vcc
	s_cbranch_execz .LBB0_43
	v_and_b32_e32 v38, 0x1fffffc, v35
	v_mov_b32_e32 v39, 0x10600
	v_add_u32_e32 v38, 0x10200, v38
	v_mov_b32_e32 v40, 1
	v_lshl_add_u32 v39, v34, 2, v39
	ds_add_rtn_u32 v18, v38, v40
	ds_add_rtn_u32 v10, v39, v40
